# v41: v40 + expert gate/up GEMM epilogue (SwiGLU) re-issued as packed f32 ops in wide stages, same per-element operations and order
# baseline (speedup 1.0000x reference)
; __device__ __forceinline__ float sigmoidf_(float x) { return __builtin_amdgcn_rcpf(1.f + __builtin_amdgcn_exp2f(-1.4426950408889634f * x)); }
; __device__ __forceinline__ unsigned pack_fp8x4(float a, float b, float c, float d) { int w = __builtin_amdgcn_cvt_pk_fp8_f32(a, b, 0, false); w = __builtin_amdgcn_cvt_pk_fp8_f32(c, d, w, true); return (unsigned)w; }
;     __device__ __forceinline__ void operator()(const f32x4 (&acc)[2][2][4][2], const Unit& u, int wr, int wc, int fr, int fq) const {
;     ...
;         const int e = u.pn >> 4, j = u.pn & 15, colL = 128 * j + wc * 32 + 8 * fq, row0 = u.pm * HALF + wr * 64 + fr;
;         f32x4 bg[2], bu[2];
; #pragma unroll
;         for (int n = 0; n < 2; ++n) { bg[n] = *(const f32x4*)(bgu + (size_t)e * 4096 + colL + 4 * n); bu[n] = *(const f32x4*)(bgu + (size_t)e * 4096 + 2048 + colL + 4 * n); }
; #pragma unroll
;         for (int ai = 0; ai < 2; ++ai) if (!(ai == 1 && u.half))
; #pragma unroll
;             for (int m = 0; m < 4; ++m) { const size_t row = (size_t)(row0 + ai * HALF + m * 16);
;                 float a[8];
; #pragma unroll
;                 for (int n = 0; n < 2; ++n)
; #pragma unroll
;                     for (int i = 0; i < 4; ++i) { float g = acc[ai][0][m][n][i] * 0.015625f + bg[n][i], up = acc[ai][1][m][n][i] * 0.015625f + bu[n][i];
;                         g = fminf(g, 7.0f); up = fminf(fmaxf(up, -7.0f), 7.0f);
;                         a[4 * n + i] = (up + 1.0f) * g * sigmoidf_(1.702f * g); }
;                 uint2 w; w.x = pack_fp8x4(a[0], a[1], a[2], a[3]); w.y = pack_fp8x4(a[4], a[5], a[6], a[7]);
.LBB0_1352:
	s_ashr_i32 s34, s30, 4
	s_lshl_b32 s21, s30, 7
	s_and_b32 s21, s21, 0x780
	s_ashr_i32 s35, s34, 31
	v_mov_b32_e32 v2, v216
	v_mov_b32_e32 v20, v1
	s_or_b32 s21, s21, s54
	s_lshl_b64 s[34:35], s[34:35], 14
	s_nop 15
	s_nop 15
	s_add_u32 s34, s78, s34
	v_lshl_add_u32 v18, v2, 3, s21
	s_addc_u32 s35, s79, s35
	v_ashrrev_i32_e32 v19, 31, v18
	v_lshl_add_u64 v[6:7], v[18:19], 2, s[34:35]
	s_movk_i32 s21, 0x2000
	v_add_co_u32_e32 v8, vcc, s21, v6
	v_mov_b64_e32 v[14:15], v[226:227]
	v_mov_b64_e32 v[16:17], v[228:229]
	v_mov_b64_e32 v[2:3], v[230:231]
	v_mov_b64_e32 v[4:5], v[232:233]
	v_addc_co_u32_e32 v9, vcc, 0, v7, vcc
	v_mov_b64_e32 v[10:11], v[234:235]
	v_mov_b64_e32 v[12:13], v[236:237]
	v_lshl_add_u64 v[6:7], v[6:7], 0, s[18:19]
	v_mov_b64_e32 v[6:7], v[238:239]
	v_mov_b64_e32 v[8:9], v[240:241]
	s_lshl_b32 s21, s71, 7
	s_add_i32 s21, s21, s53
	v_add_u32_e32 v20, s21, v20
	s_and_b64 vcc, exec, s[2:3]
	s_waitcnt lgkmcnt(0)
	v_mov_b32_e32 v2, 0x3c800000
	v_mov_b32_e32 v4, 0x3fd9db23
	v_mov_b32_e32 v6, 0xbfb8aa3b
	v_pk_fma_f32 v[194:195], v[194:195], v[2:3], v[226:227] op_sel_hi:[1,0,1]
	v_pk_fma_f32 v[196:197], v[196:197], v[2:3], v[228:229] op_sel_hi:[1,0,1]
	v_pk_fma_f32 v[186:187], v[186:187], v[2:3], v[230:231] op_sel_hi:[1,0,1]
	v_pk_fma_f32 v[188:189], v[188:189], v[2:3], v[232:233] op_sel_hi:[1,0,1]
	v_pk_fma_f32 v[190:191], v[190:191], v[2:3], v[234:235] op_sel_hi:[1,0,1]
	v_pk_fma_f32 v[192:193], v[192:193], v[2:3], v[236:237] op_sel_hi:[1,0,1]
	v_pk_fma_f32 v[182:183], v[182:183], v[2:3], v[238:239] op_sel_hi:[1,0,1]
	v_pk_fma_f32 v[184:185], v[184:185], v[2:3], v[240:241] op_sel_hi:[1,0,1]
	v_pk_fma_f32 v[178:179], v[178:179], v[2:3], v[226:227] op_sel_hi:[1,0,1]
	v_pk_fma_f32 v[180:181], v[180:181], v[2:3], v[228:229] op_sel_hi:[1,0,1]
	v_pk_fma_f32 v[170:171], v[170:171], v[2:3], v[230:231] op_sel_hi:[1,0,1]
	v_pk_fma_f32 v[172:173], v[172:173], v[2:3], v[232:233] op_sel_hi:[1,0,1]
	v_pk_fma_f32 v[174:175], v[174:175], v[2:3], v[234:235] op_sel_hi:[1,0,1]
	v_pk_fma_f32 v[176:177], v[176:177], v[2:3], v[236:237] op_sel_hi:[1,0,1]
	v_pk_fma_f32 v[166:167], v[166:167], v[2:3], v[238:239] op_sel_hi:[1,0,1]
	v_pk_fma_f32 v[168:169], v[168:169], v[2:3], v[240:241] op_sel_hi:[1,0,1]
	v_min_f32_e32 v194, 0x40e00000, v194
	v_min_f32_e32 v195, 0x40e00000, v195
	v_min_f32_e32 v196, 0x40e00000, v196
	v_min_f32_e32 v197, 0x40e00000, v197
	v_min_f32_e32 v186, 0x40e00000, v186
	v_min_f32_e32 v187, 0x40e00000, v187
	v_min_f32_e32 v188, 0x40e00000, v188
	v_min_f32_e32 v189, 0x40e00000, v189
	v_med3_f32 v190, v190, s68, v221
	v_med3_f32 v191, v191, s68, v221
	v_med3_f32 v192, v192, s68, v221
	v_med3_f32 v193, v193, s68, v221
	v_med3_f32 v182, v182, s68, v221
	v_med3_f32 v183, v183, s68, v221
	v_med3_f32 v184, v184, s68, v221
	v_med3_f32 v185, v185, s68, v221
	v_min_f32_e32 v178, 0x40e00000, v178
	v_min_f32_e32 v179, 0x40e00000, v179
	v_min_f32_e32 v180, 0x40e00000, v180
	v_min_f32_e32 v181, 0x40e00000, v181
	v_min_f32_e32 v170, 0x40e00000, v170
	v_min_f32_e32 v171, 0x40e00000, v171
	v_min_f32_e32 v172, 0x40e00000, v172
	v_min_f32_e32 v173, 0x40e00000, v173
	v_med3_f32 v174, v174, s68, v221
	v_med3_f32 v175, v175, s68, v221
	v_med3_f32 v176, v176, s68, v221
	v_med3_f32 v177, v177, s68, v221
	v_med3_f32 v166, v166, s68, v221
	v_med3_f32 v167, v167, s68, v221
	v_med3_f32 v168, v168, s68, v221
	v_med3_f32 v169, v169, s68, v221
	v_pk_add_f32 v[190:191], v[190:191], 1.0 op_sel_hi:[1,0]
	v_pk_add_f32 v[192:193], v[192:193], 1.0 op_sel_hi:[1,0]
	v_pk_add_f32 v[182:183], v[182:183], 1.0 op_sel_hi:[1,0]
	v_pk_add_f32 v[184:185], v[184:185], 1.0 op_sel_hi:[1,0]
	v_pk_mul_f32 v[22:23], v[194:195], v[4:5] op_sel_hi:[1,0]
	v_pk_mul_f32 v[24:25], v[196:197], v[4:5] op_sel_hi:[1,0]
	v_pk_mul_f32 v[26:27], v[186:187], v[4:5] op_sel_hi:[1,0]
	v_pk_mul_f32 v[28:29], v[188:189], v[4:5] op_sel_hi:[1,0]
	v_pk_add_f32 v[174:175], v[174:175], 1.0 op_sel_hi:[1,0]
	v_pk_add_f32 v[176:177], v[176:177], 1.0 op_sel_hi:[1,0]
	v_pk_add_f32 v[166:167], v[166:167], 1.0 op_sel_hi:[1,0]
	v_pk_add_f32 v[168:169], v[168:169], 1.0 op_sel_hi:[1,0]
	v_pk_mul_f32 v[30:31], v[178:179], v[4:5] op_sel_hi:[1,0]
	v_pk_mul_f32 v[32:33], v[180:181], v[4:5] op_sel_hi:[1,0]
	v_pk_mul_f32 v[34:35], v[170:171], v[4:5] op_sel_hi:[1,0]
	v_pk_mul_f32 v[36:37], v[172:173], v[4:5] op_sel_hi:[1,0]
	v_pk_mul_f32 v[22:23], v[22:23], v[6:7] op_sel_hi:[1,0]
	v_pk_mul_f32 v[24:25], v[24:25], v[6:7] op_sel_hi:[1,0]
	v_pk_mul_f32 v[26:27], v[26:27], v[6:7] op_sel_hi:[1,0]
	v_pk_mul_f32 v[28:29], v[28:29], v[6:7] op_sel_hi:[1,0]
	v_pk_mul_f32 v[30:31], v[30:31], v[6:7] op_sel_hi:[1,0]
	v_pk_mul_f32 v[32:33], v[32:33], v[6:7] op_sel_hi:[1,0]
	v_pk_mul_f32 v[34:35], v[34:35], v[6:7] op_sel_hi:[1,0]
	v_pk_mul_f32 v[36:37], v[36:37], v[6:7] op_sel_hi:[1,0]
	v_exp_f32_e32 v22, v22
	v_exp_f32_e32 v23, v23
	v_exp_f32_e32 v24, v24
	v_exp_f32_e32 v25, v25
	v_exp_f32_e32 v26, v26
	v_exp_f32_e32 v27, v27
	v_exp_f32_e32 v28, v28
	v_exp_f32_e32 v29, v29
	v_exp_f32_e32 v30, v30
	v_exp_f32_e32 v31, v31
	v_exp_f32_e32 v32, v32
	v_exp_f32_e32 v33, v33
	v_exp_f32_e32 v34, v34
	v_exp_f32_e32 v35, v35
	v_exp_f32_e32 v36, v36
	v_exp_f32_e32 v37, v37
	v_pk_mul_f32 v[194:195], v[194:195], v[190:191]
	v_pk_mul_f32 v[196:197], v[196:197], v[192:193]
	v_pk_mul_f32 v[186:187], v[186:187], v[182:183]
	v_pk_mul_f32 v[188:189], v[188:189], v[184:185]
	v_pk_mul_f32 v[178:179], v[178:179], v[174:175]
	v_pk_mul_f32 v[180:181], v[180:181], v[176:177]
	v_pk_mul_f32 v[170:171], v[170:171], v[166:167]
	v_pk_mul_f32 v[172:173], v[172:173], v[168:169]
	v_pk_add_f32 v[22:23], v[22:23], 1.0 op_sel_hi:[1,0]
; __device__ __forceinline__ float sigmoidf_(float x) { return __builtin_amdgcn_rcpf(1.f + __builtin_amdgcn_exp2f(-1.4426950408889634f * x)); }
; __device__ __forceinline__ unsigned pack_fp8x4(float a, float b, float c, float d) { int w = __builtin_amdgcn_cvt_pk_fp8_f32(a, b, 0, false); w = __builtin_amdgcn_cvt_pk_fp8_f32(c, d, w, true); return (unsigned)w; }
; #define ACT(t) (KBASE(t) <= qlo + QBLK - 1 && KBASE(t) + KVBLK - 1 >= qlo - W + 1)
;     __device__ __forceinline__ void operator()(const f32x4 (&acc)[2][2][4][2], const Unit& u, int wr, int wc, int fr, int fq) const {
;     ...
; #pragma unroll
;                 for (int n = 0; n < 2; ++n)
; #pragma unroll
;                     for (int i = 0; i < 4; ++i) { float g = acc[ai][0][m][n][i] * 0.015625f + bg[n][i], up = acc[ai][1][m][n][i] * 0.015625f + bu[n][i];
;                         g = fminf(g, 7.0f); up = fminf(fmaxf(up, -7.0f), 7.0f);
;                         a[4 * n + i] = (up + 1.0f) * g * sigmoidf_(1.702f * g); }
;                 uint2 w; w.x = pack_fp8x4(a[0], a[1], a[2], a[3]); w.y = pack_fp8x4(a[4], a[5], a[6], a[7]);
;                 *(uint2*)(ACT + row * 2048 + colL) = w; }
	v_pk_add_f32 v[24:25], v[24:25], 1.0 op_sel_hi:[1,0]
	v_pk_add_f32 v[26:27], v[26:27], 1.0 op_sel_hi:[1,0]
	v_pk_add_f32 v[28:29], v[28:29], 1.0 op_sel_hi:[1,0]
	v_pk_add_f32 v[30:31], v[30:31], 1.0 op_sel_hi:[1,0]
	v_pk_add_f32 v[32:33], v[32:33], 1.0 op_sel_hi:[1,0]
	v_pk_add_f32 v[34:35], v[34:35], 1.0 op_sel_hi:[1,0]
	v_pk_add_f32 v[36:37], v[36:37], 1.0 op_sel_hi:[1,0]
	v_rcp_f32_e32 v22, v22
	v_rcp_f32_e32 v23, v23
	v_rcp_f32_e32 v24, v24
	v_rcp_f32_e32 v25, v25
	v_rcp_f32_e32 v26, v26
	v_rcp_f32_e32 v27, v27
	v_rcp_f32_e32 v28, v28
	v_rcp_f32_e32 v29, v29
	v_rcp_f32_e32 v30, v30
	v_rcp_f32_e32 v31, v31
	v_rcp_f32_e32 v32, v32
	v_rcp_f32_e32 v33, v33
	v_rcp_f32_e32 v34, v34
	v_rcp_f32_e32 v35, v35
	v_rcp_f32_e32 v36, v36
	v_rcp_f32_e32 v37, v37
	v_mov_b32_e32 v12, v20
	v_ashrrev_i32_e32 v13, 31, v12
	v_lshlrev_b64 v[12:13], 11, v[12:13]
	v_lshl_add_u64 v[12:13], s[6:7], 0, v[12:13]
	v_lshl_add_u64 v[12:13], v[12:13], 0, v[18:19]
	v_add_u32_e32 v14, 0x10, v20
	v_ashrrev_i32_e32 v15, 31, v14
	v_lshlrev_b64 v[14:15], 11, v[14:15]
	v_lshl_add_u64 v[14:15], s[6:7], 0, v[14:15]
	v_lshl_add_u64 v[14:15], v[14:15], 0, v[18:19]
	v_pk_mul_f32 v[194:195], v[194:195], v[22:23]
	v_pk_mul_f32 v[196:197], v[196:197], v[24:25]
	v_pk_mul_f32 v[186:187], v[186:187], v[26:27]
	v_pk_mul_f32 v[188:189], v[188:189], v[28:29]
	v_pk_mul_f32 v[178:179], v[178:179], v[30:31]
	v_pk_mul_f32 v[180:181], v[180:181], v[32:33]
	v_pk_mul_f32 v[170:171], v[170:171], v[34:35]
	v_pk_mul_f32 v[172:173], v[172:173], v[36:37]
	v_cvt_pk_fp8_f32 v8, v194, v195
	v_cvt_pk_fp8_f32 v9, v186, v187
	v_cvt_pk_fp8_f32 v8, v196, v197 op_sel:[0,0,1]
	v_cvt_pk_fp8_f32 v9, v188, v189 op_sel:[0,0,1]
	v_cvt_pk_fp8_f32 v10, v178, v179
	v_cvt_pk_fp8_f32 v11, v170, v171
	v_cvt_pk_fp8_f32 v10, v180, v181 op_sel:[0,0,1]
	v_cvt_pk_fp8_f32 v11, v172, v173 op_sel:[0,0,1]
	s_nop 0
	global_store_dwordx2 v[12:13], v[8:9], off
	global_store_dwordx2 v[14:15], v[10:11], off
	v_pk_fma_f32 v[162:163], v[162:163], v[2:3], v[226:227] op_sel_hi:[1,0,1]
	v_pk_fma_f32 v[164:165], v[164:165], v[2:3], v[228:229] op_sel_hi:[1,0,1]
	v_pk_fma_f32 v[154:155], v[154:155], v[2:3], v[230:231] op_sel_hi:[1,0,1]
	v_pk_fma_f32 v[156:157], v[156:157], v[2:3], v[232:233] op_sel_hi:[1,0,1]
	v_pk_fma_f32 v[158:159], v[158:159], v[2:3], v[234:235] op_sel_hi:[1,0,1]
	v_pk_fma_f32 v[160:161], v[160:161], v[2:3], v[236:237] op_sel_hi:[1,0,1]
	v_pk_fma_f32 v[150:151], v[150:151], v[2:3], v[238:239] op_sel_hi:[1,0,1]
	v_pk_fma_f32 v[152:153], v[152:153], v[2:3], v[240:241] op_sel_hi:[1,0,1]
	v_pk_fma_f32 v[146:147], v[146:147], v[2:3], v[226:227] op_sel_hi:[1,0,1]
	v_pk_fma_f32 v[148:149], v[148:149], v[2:3], v[228:229] op_sel_hi:[1,0,1]
	v_pk_fma_f32 v[138:139], v[138:139], v[2:3], v[230:231] op_sel_hi:[1,0,1]
	v_pk_fma_f32 v[140:141], v[140:141], v[2:3], v[232:233] op_sel_hi:[1,0,1]
	v_pk_fma_f32 v[142:143], v[142:143], v[2:3], v[234:235] op_sel_hi:[1,0,1]
	v_pk_fma_f32 v[144:145], v[144:145], v[2:3], v[236:237] op_sel_hi:[1,0,1]
	v_pk_fma_f32 v[134:135], v[134:135], v[2:3], v[238:239] op_sel_hi:[1,0,1]
	v_pk_fma_f32 v[136:137], v[136:137], v[2:3], v[240:241] op_sel_hi:[1,0,1]
	v_min_f32_e32 v162, 0x40e00000, v162
	v_min_f32_e32 v163, 0x40e00000, v163
	v_min_f32_e32 v164, 0x40e00000, v164
	v_min_f32_e32 v165, 0x40e00000, v165
	v_min_f32_e32 v154, 0x40e00000, v154
	v_min_f32_e32 v155, 0x40e00000, v155
	v_min_f32_e32 v156, 0x40e00000, v156
	v_min_f32_e32 v157, 0x40e00000, v157
	v_med3_f32 v158, v158, s68, v221
	v_med3_f32 v159, v159, s68, v221
	v_med3_f32 v160, v160, s68, v221
	v_med3_f32 v161, v161, s68, v221
	v_med3_f32 v150, v150, s68, v221
	v_med3_f32 v151, v151, s68, v221
	v_med3_f32 v152, v152, s68, v221
	v_med3_f32 v153, v153, s68, v221
	v_min_f32_e32 v146, 0x40e00000, v146
	v_min_f32_e32 v147, 0x40e00000, v147
	v_min_f32_e32 v148, 0x40e00000, v148
	v_min_f32_e32 v149, 0x40e00000, v149
	v_min_f32_e32 v138, 0x40e00000, v138
	v_min_f32_e32 v139, 0x40e00000, v139
	v_min_f32_e32 v140, 0x40e00000, v140
	v_min_f32_e32 v141, 0x40e00000, v141
	v_med3_f32 v142, v142, s68, v221
	v_med3_f32 v143, v143, s68, v221
	v_med3_f32 v144, v144, s68, v221
	v_med3_f32 v145, v145, s68, v221
	v_med3_f32 v134, v134, s68, v221
	v_med3_f32 v135, v135, s68, v221
	v_med3_f32 v136, v136, s68, v221
	v_med3_f32 v137, v137, s68, v221
; __device__ __forceinline__ float sigmoidf_(float x) { return __builtin_amdgcn_rcpf(1.f + __builtin_amdgcn_exp2f(-1.4426950408889634f * x)); }
; __device__ __forceinline__ unsigned pack_fp8x4(float a, float b, float c, float d) { int w = __builtin_amdgcn_cvt_pk_fp8_f32(a, b, 0, false); w = __builtin_amdgcn_cvt_pk_fp8_f32(c, d, w, true); return (unsigned)w; }
; #define ACT(t) (KBASE(t) <= qlo + QBLK - 1 && KBASE(t) + KVBLK - 1 >= qlo - W + 1)
;     __device__ __forceinline__ void operator()(const f32x4 (&acc)[2][2][4][2], const Unit& u, int wr, int wc, int fr, int fq) const {
;     ...
; #pragma unroll
;                 for (int n = 0; n < 2; ++n)
; #pragma unroll
;                     for (int i = 0; i < 4; ++i) { float g = acc[ai][0][m][n][i] * 0.015625f + bg[n][i], up = acc[ai][1][m][n][i] * 0.015625f + bu[n][i];
;                         g = fminf(g, 7.0f); up = fminf(fmaxf(up, -7.0f), 7.0f);
;                         a[4 * n + i] = (up + 1.0f) * g * sigmoidf_(1.702f * g); }
;                 uint2 w; w.x = pack_fp8x4(a[0], a[1], a[2], a[3]); w.y = pack_fp8x4(a[4], a[5], a[6], a[7]);
;                 *(uint2*)(ACT + row * 2048 + colL) = w; }
	v_pk_add_f32 v[158:159], v[158:159], 1.0 op_sel_hi:[1,0]
	v_pk_add_f32 v[160:161], v[160:161], 1.0 op_sel_hi:[1,0]
	v_pk_add_f32 v[150:151], v[150:151], 1.0 op_sel_hi:[1,0]
	v_pk_add_f32 v[152:153], v[152:153], 1.0 op_sel_hi:[1,0]
	v_pk_mul_f32 v[22:23], v[162:163], v[4:5] op_sel_hi:[1,0]
	v_pk_mul_f32 v[24:25], v[164:165], v[4:5] op_sel_hi:[1,0]
	v_pk_mul_f32 v[26:27], v[154:155], v[4:5] op_sel_hi:[1,0]
	v_pk_mul_f32 v[28:29], v[156:157], v[4:5] op_sel_hi:[1,0]
	v_pk_add_f32 v[142:143], v[142:143], 1.0 op_sel_hi:[1,0]
	v_pk_add_f32 v[144:145], v[144:145], 1.0 op_sel_hi:[1,0]
	v_pk_add_f32 v[134:135], v[134:135], 1.0 op_sel_hi:[1,0]
	v_pk_add_f32 v[136:137], v[136:137], 1.0 op_sel_hi:[1,0]
	v_pk_mul_f32 v[30:31], v[146:147], v[4:5] op_sel_hi:[1,0]
	v_pk_mul_f32 v[32:33], v[148:149], v[4:5] op_sel_hi:[1,0]
	v_pk_mul_f32 v[34:35], v[138:139], v[4:5] op_sel_hi:[1,0]
	v_pk_mul_f32 v[36:37], v[140:141], v[4:5] op_sel_hi:[1,0]
	v_pk_mul_f32 v[22:23], v[22:23], v[6:7] op_sel_hi:[1,0]
	v_pk_mul_f32 v[24:25], v[24:25], v[6:7] op_sel_hi:[1,0]
	v_pk_mul_f32 v[26:27], v[26:27], v[6:7] op_sel_hi:[1,0]
	v_pk_mul_f32 v[28:29], v[28:29], v[6:7] op_sel_hi:[1,0]
	v_pk_mul_f32 v[30:31], v[30:31], v[6:7] op_sel_hi:[1,0]
	v_pk_mul_f32 v[32:33], v[32:33], v[6:7] op_sel_hi:[1,0]
	v_pk_mul_f32 v[34:35], v[34:35], v[6:7] op_sel_hi:[1,0]
	v_pk_mul_f32 v[36:37], v[36:37], v[6:7] op_sel_hi:[1,0]
	v_exp_f32_e32 v22, v22
	v_exp_f32_e32 v23, v23
	v_exp_f32_e32 v24, v24
	v_exp_f32_e32 v25, v25
	v_exp_f32_e32 v26, v26
	v_exp_f32_e32 v27, v27
	v_exp_f32_e32 v28, v28
	v_exp_f32_e32 v29, v29
	v_exp_f32_e32 v30, v30
	v_exp_f32_e32 v31, v31
	v_exp_f32_e32 v32, v32
	v_exp_f32_e32 v33, v33
	v_exp_f32_e32 v34, v34
	v_exp_f32_e32 v35, v35
	v_exp_f32_e32 v36, v36
	v_exp_f32_e32 v37, v37
	v_pk_mul_f32 v[162:163], v[162:163], v[158:159]
	v_pk_mul_f32 v[164:165], v[164:165], v[160:161]
	v_pk_mul_f32 v[154:155], v[154:155], v[150:151]
	v_pk_mul_f32 v[156:157], v[156:157], v[152:153]
	v_pk_mul_f32 v[146:147], v[146:147], v[142:143]
	v_pk_mul_f32 v[148:149], v[148:149], v[144:145]
	v_pk_mul_f32 v[138:139], v[138:139], v[134:135]
	v_pk_mul_f32 v[140:141], v[140:141], v[136:137]
	v_pk_add_f32 v[22:23], v[22:23], 1.0 op_sel_hi:[1,0]
	v_pk_add_f32 v[24:25], v[24:25], 1.0 op_sel_hi:[1,0]
	v_pk_add_f32 v[26:27], v[26:27], 1.0 op_sel_hi:[1,0]
	v_pk_add_f32 v[28:29], v[28:29], 1.0 op_sel_hi:[1,0]
	v_pk_add_f32 v[30:31], v[30:31], 1.0 op_sel_hi:[1,0]
	v_pk_add_f32 v[32:33], v[32:33], 1.0 op_sel_hi:[1,0]
	v_pk_add_f32 v[34:35], v[34:35], 1.0 op_sel_hi:[1,0]
	v_pk_add_f32 v[36:37], v[36:37], 1.0 op_sel_hi:[1,0]
	v_rcp_f32_e32 v22, v22
	v_rcp_f32_e32 v23, v23
	v_rcp_f32_e32 v24, v24
	v_rcp_f32_e32 v25, v25
	v_rcp_f32_e32 v26, v26
	v_rcp_f32_e32 v27, v27
	v_rcp_f32_e32 v28, v28
	v_rcp_f32_e32 v29, v29
	v_rcp_f32_e32 v30, v30
	v_rcp_f32_e32 v31, v31
	v_rcp_f32_e32 v32, v32
	v_rcp_f32_e32 v33, v33
	v_rcp_f32_e32 v34, v34
	v_rcp_f32_e32 v35, v35
	v_rcp_f32_e32 v36, v36
	v_rcp_f32_e32 v37, v37
	v_add_u32_e32 v12, 0x20, v20
	v_ashrrev_i32_e32 v13, 31, v12
	v_lshlrev_b64 v[12:13], 11, v[12:13]
	v_lshl_add_u64 v[12:13], s[6:7], 0, v[12:13]
	v_lshl_add_u64 v[12:13], v[12:13], 0, v[18:19]
	v_add_u32_e32 v14, 0x30, v20
	v_ashrrev_i32_e32 v15, 31, v14
	v_lshlrev_b64 v[14:15], 11, v[14:15]
	v_lshl_add_u64 v[14:15], s[6:7], 0, v[14:15]
	v_lshl_add_u64 v[14:15], v[14:15], 0, v[18:19]
	v_pk_mul_f32 v[162:163], v[162:163], v[22:23]
	v_pk_mul_f32 v[164:165], v[164:165], v[24:25]
	v_pk_mul_f32 v[154:155], v[154:155], v[26:27]
	v_pk_mul_f32 v[156:157], v[156:157], v[28:29]
	v_pk_mul_f32 v[146:147], v[146:147], v[30:31]
	v_pk_mul_f32 v[148:149], v[148:149], v[32:33]
	v_pk_mul_f32 v[138:139], v[138:139], v[34:35]
	v_pk_mul_f32 v[140:141], v[140:141], v[36:37]
	v_cvt_pk_fp8_f32 v8, v162, v163
	v_cvt_pk_fp8_f32 v9, v154, v155
	v_cvt_pk_fp8_f32 v8, v164, v165 op_sel:[0,0,1]
	v_cvt_pk_fp8_f32 v9, v156, v157 op_sel:[0,0,1]
	v_cvt_pk_fp8_f32 v10, v146, v147
	v_cvt_pk_fp8_f32 v11, v138, v139
	v_cvt_pk_fp8_f32 v10, v148, v149 op_sel:[0,0,1]
	v_cvt_pk_fp8_f32 v11, v140, v141 op_sel:[0,0,1]
	s_nop 0
	global_store_dwordx2 v[12:13], v[8:9], off
	global_store_dwordx2 v[14:15], v[10:11], off
	s_cbranch_vccz .LBB0_1355
	s_andn2_b64 vcc, exec, s[26:27]
	s_mov_b64 s[2:3], -1
	s_cbranch_vccnz .LBB0_1334
	s_branch .LBB0_1356

; __device__ __forceinline__ float sigmoidf_(float x) { return __builtin_amdgcn_rcpf(1.f + __builtin_amdgcn_exp2f(-1.4426950408889634f * x)); }
; __device__ __forceinline__ unsigned pack_fp8x4(float a, float b, float c, float d) { int w = __builtin_amdgcn_cvt_pk_fp8_f32(a, b, 0, false); w = __builtin_amdgcn_cvt_pk_fp8_f32(c, d, w, true); return (unsigned)w; }
;     __device__ __forceinline__ void operator()(const f32x4 (&acc)[2][2][4][2], const Unit& u, int wr, int wc, int fr, int fq) const {
;     ...
;         for (int ai = 0; ai < 2; ++ai) if (!(ai == 1 && u.half))
; #pragma unroll
;             for (int m = 0; m < 4; ++m) { const size_t row = (size_t)(row0 + ai * HALF + m * 16);
;                 float a[8];
; #pragma unroll
;                 for (int n = 0; n < 2; ++n)
; #pragma unroll
;                     for (int i = 0; i < 4; ++i) { float g = acc[ai][0][m][n][i] * 0.015625f + bg[n][i], up = acc[ai][1][m][n][i] * 0.015625f + bu[n][i];
;                         g = fminf(g, 7.0f); up = fminf(fmaxf(up, -7.0f), 7.0f);
;                         a[4 * n + i] = (up + 1.0f) * g * sigmoidf_(1.702f * g); }
;                 uint2 w; w.x = pack_fp8x4(a[0], a[1], a[2], a[3]); w.y = pack_fp8x4(a[4], a[5], a[6], a[7]);
.LBB0_1355:
	v_mov_b32_e32 v2, 0x3c800000
	v_mov_b32_e32 v4, 0x3fd9db23
	v_mov_b32_e32 v6, 0xbfb8aa3b
	v_pk_fma_f32 v[130:131], v[130:131], v[2:3], v[226:227] op_sel_hi:[1,0,1]
	v_pk_fma_f32 v[132:133], v[132:133], v[2:3], v[228:229] op_sel_hi:[1,0,1]
	v_pk_fma_f32 v[122:123], v[122:123], v[2:3], v[230:231] op_sel_hi:[1,0,1]
	v_pk_fma_f32 v[124:125], v[124:125], v[2:3], v[232:233] op_sel_hi:[1,0,1]
	v_pk_fma_f32 v[126:127], v[126:127], v[2:3], v[234:235] op_sel_hi:[1,0,1]
	v_pk_fma_f32 v[128:129], v[128:129], v[2:3], v[236:237] op_sel_hi:[1,0,1]
	v_pk_fma_f32 v[118:119], v[118:119], v[2:3], v[238:239] op_sel_hi:[1,0,1]
	v_pk_fma_f32 v[120:121], v[120:121], v[2:3], v[240:241] op_sel_hi:[1,0,1]
	v_pk_fma_f32 v[114:115], v[114:115], v[2:3], v[226:227] op_sel_hi:[1,0,1]
	v_pk_fma_f32 v[116:117], v[116:117], v[2:3], v[228:229] op_sel_hi:[1,0,1]
	v_pk_fma_f32 v[106:107], v[106:107], v[2:3], v[230:231] op_sel_hi:[1,0,1]
	v_pk_fma_f32 v[108:109], v[108:109], v[2:3], v[232:233] op_sel_hi:[1,0,1]
	v_pk_fma_f32 v[110:111], v[110:111], v[2:3], v[234:235] op_sel_hi:[1,0,1]
	v_pk_fma_f32 v[112:113], v[112:113], v[2:3], v[236:237] op_sel_hi:[1,0,1]
	v_pk_fma_f32 v[102:103], v[102:103], v[2:3], v[238:239] op_sel_hi:[1,0,1]
	v_pk_fma_f32 v[104:105], v[104:105], v[2:3], v[240:241] op_sel_hi:[1,0,1]
	v_min_f32_e32 v130, 0x40e00000, v130
	v_min_f32_e32 v131, 0x40e00000, v131
	v_min_f32_e32 v132, 0x40e00000, v132
	v_min_f32_e32 v133, 0x40e00000, v133
	v_min_f32_e32 v122, 0x40e00000, v122
	v_min_f32_e32 v123, 0x40e00000, v123
	v_min_f32_e32 v124, 0x40e00000, v124
	v_min_f32_e32 v125, 0x40e00000, v125
	v_med3_f32 v126, v126, s68, v221
	v_med3_f32 v127, v127, s68, v221
	v_med3_f32 v128, v128, s68, v221
	v_med3_f32 v129, v129, s68, v221
	v_med3_f32 v118, v118, s68, v221
	v_med3_f32 v119, v119, s68, v221
	v_med3_f32 v120, v120, s68, v221
	v_med3_f32 v121, v121, s68, v221
	v_min_f32_e32 v114, 0x40e00000, v114
	v_min_f32_e32 v115, 0x40e00000, v115
	v_min_f32_e32 v116, 0x40e00000, v116
	v_min_f32_e32 v117, 0x40e00000, v117
	v_min_f32_e32 v106, 0x40e00000, v106
	v_min_f32_e32 v107, 0x40e00000, v107
	v_min_f32_e32 v108, 0x40e00000, v108
	v_min_f32_e32 v109, 0x40e00000, v109
	v_med3_f32 v110, v110, s68, v221
	v_med3_f32 v111, v111, s68, v221
	v_med3_f32 v112, v112, s68, v221
	v_med3_f32 v113, v113, s68, v221
	v_med3_f32 v102, v102, s68, v221
	v_med3_f32 v103, v103, s68, v221
	v_med3_f32 v104, v104, s68, v221
	v_med3_f32 v105, v105, s68, v221
	v_pk_add_f32 v[126:127], v[126:127], 1.0 op_sel_hi:[1,0]
	v_pk_add_f32 v[128:129], v[128:129], 1.0 op_sel_hi:[1,0]
	v_pk_add_f32 v[118:119], v[118:119], 1.0 op_sel_hi:[1,0]
	v_pk_add_f32 v[120:121], v[120:121], 1.0 op_sel_hi:[1,0]
	v_pk_mul_f32 v[22:23], v[130:131], v[4:5] op_sel_hi:[1,0]
	v_pk_mul_f32 v[24:25], v[132:133], v[4:5] op_sel_hi:[1,0]
	v_pk_mul_f32 v[26:27], v[122:123], v[4:5] op_sel_hi:[1,0]
	v_pk_mul_f32 v[28:29], v[124:125], v[4:5] op_sel_hi:[1,0]
	v_pk_add_f32 v[110:111], v[110:111], 1.0 op_sel_hi:[1,0]
	v_pk_add_f32 v[112:113], v[112:113], 1.0 op_sel_hi:[1,0]
	v_pk_add_f32 v[102:103], v[102:103], 1.0 op_sel_hi:[1,0]
	v_pk_add_f32 v[104:105], v[104:105], 1.0 op_sel_hi:[1,0]
	v_pk_mul_f32 v[30:31], v[114:115], v[4:5] op_sel_hi:[1,0]
	v_pk_mul_f32 v[32:33], v[116:117], v[4:5] op_sel_hi:[1,0]
	v_pk_mul_f32 v[34:35], v[106:107], v[4:5] op_sel_hi:[1,0]
	v_pk_mul_f32 v[36:37], v[108:109], v[4:5] op_sel_hi:[1,0]
	v_pk_mul_f32 v[22:23], v[22:23], v[6:7] op_sel_hi:[1,0]
	v_pk_mul_f32 v[24:25], v[24:25], v[6:7] op_sel_hi:[1,0]
	v_pk_mul_f32 v[26:27], v[26:27], v[6:7] op_sel_hi:[1,0]
	v_pk_mul_f32 v[28:29], v[28:29], v[6:7] op_sel_hi:[1,0]
	v_pk_mul_f32 v[30:31], v[30:31], v[6:7] op_sel_hi:[1,0]
	v_pk_mul_f32 v[32:33], v[32:33], v[6:7] op_sel_hi:[1,0]
	v_pk_mul_f32 v[34:35], v[34:35], v[6:7] op_sel_hi:[1,0]
	v_pk_mul_f32 v[36:37], v[36:37], v[6:7] op_sel_hi:[1,0]
	v_exp_f32_e32 v22, v22
	v_exp_f32_e32 v23, v23
	v_exp_f32_e32 v24, v24
	v_exp_f32_e32 v25, v25
	v_exp_f32_e32 v26, v26
	v_exp_f32_e32 v27, v27
	v_exp_f32_e32 v28, v28
	v_exp_f32_e32 v29, v29
	v_exp_f32_e32 v30, v30
	v_exp_f32_e32 v31, v31
	v_exp_f32_e32 v32, v32
	v_exp_f32_e32 v33, v33
	v_exp_f32_e32 v34, v34
	v_exp_f32_e32 v35, v35
	v_exp_f32_e32 v36, v36
	v_exp_f32_e32 v37, v37
	v_pk_mul_f32 v[130:131], v[130:131], v[126:127]
	v_pk_mul_f32 v[132:133], v[132:133], v[128:129]
	v_pk_mul_f32 v[122:123], v[122:123], v[118:119]
	v_pk_mul_f32 v[124:125], v[124:125], v[120:121]
	v_pk_mul_f32 v[114:115], v[114:115], v[110:111]
	v_pk_mul_f32 v[116:117], v[116:117], v[112:113]
	v_pk_mul_f32 v[106:107], v[106:107], v[102:103]
	v_pk_mul_f32 v[108:109], v[108:109], v[104:105]
	v_pk_add_f32 v[22:23], v[22:23], 1.0 op_sel_hi:[1,0]
	v_pk_add_f32 v[24:25], v[24:25], 1.0 op_sel_hi:[1,0]
	v_pk_add_f32 v[26:27], v[26:27], 1.0 op_sel_hi:[1,0]
	v_pk_add_f32 v[28:29], v[28:29], 1.0 op_sel_hi:[1,0]
	v_pk_add_f32 v[30:31], v[30:31], 1.0 op_sel_hi:[1,0]
	v_pk_add_f32 v[32:33], v[32:33], 1.0 op_sel_hi:[1,0]
	v_pk_add_f32 v[34:35], v[34:35], 1.0 op_sel_hi:[1,0]
	v_pk_add_f32 v[36:37], v[36:37], 1.0 op_sel_hi:[1,0]
	v_rcp_f32_e32 v22, v22
	v_rcp_f32_e32 v23, v23
	v_rcp_f32_e32 v24, v24
	v_rcp_f32_e32 v25, v25
	v_rcp_f32_e32 v26, v26
	v_rcp_f32_e32 v27, v27
	v_rcp_f32_e32 v28, v28
	v_rcp_f32_e32 v29, v29
	v_rcp_f32_e32 v30, v30
	v_rcp_f32_e32 v31, v31
	v_rcp_f32_e32 v32, v32
	v_rcp_f32_e32 v33, v33
	v_rcp_f32_e32 v34, v34
	v_rcp_f32_e32 v35, v35
	v_rcp_f32_e32 v36, v36
	v_rcp_f32_e32 v37, v37
	v_add_u32_e32 v12, 0x80, v20
	v_ashrrev_i32_e32 v13, 31, v12
	v_lshlrev_b64 v[12:13], 11, v[12:13]
	v_lshl_add_u64 v[12:13], s[6:7], 0, v[12:13]
	v_lshl_add_u64 v[12:13], v[12:13], 0, v[18:19]
; __device__ __forceinline__ float sigmoidf_(float x) { return __builtin_amdgcn_rcpf(1.f + __builtin_amdgcn_exp2f(-1.4426950408889634f * x)); }
; __device__ __forceinline__ unsigned pack_fp8x4(float a, float b, float c, float d) { int w = __builtin_amdgcn_cvt_pk_fp8_f32(a, b, 0, false); w = __builtin_amdgcn_cvt_pk_fp8_f32(c, d, w, true); return (unsigned)w; }
; #define ACT(t) (KBASE(t) <= qlo + QBLK - 1 && KBASE(t) + KVBLK - 1 >= qlo - W + 1)
;     __device__ __forceinline__ void operator()(const f32x4 (&acc)[2][2][4][2], const Unit& u, int wr, int wc, int fr, int fq) const {
;     ...
; #pragma unroll
;                 for (int n = 0; n < 2; ++n)
; #pragma unroll
;                     for (int i = 0; i < 4; ++i) { float g = acc[ai][0][m][n][i] * 0.015625f + bg[n][i], up = acc[ai][1][m][n][i] * 0.015625f + bu[n][i];
;                         g = fminf(g, 7.0f); up = fminf(fmaxf(up, -7.0f), 7.0f);
;                         a[4 * n + i] = (up + 1.0f) * g * sigmoidf_(1.702f * g); }
;                 uint2 w; w.x = pack_fp8x4(a[0], a[1], a[2], a[3]); w.y = pack_fp8x4(a[4], a[5], a[6], a[7]);
;                 *(uint2*)(ACT + row * 2048 + colL) = w; }
	v_add_u32_e32 v14, 0x90, v20
	v_ashrrev_i32_e32 v15, 31, v14
	v_lshlrev_b64 v[14:15], 11, v[14:15]
	v_lshl_add_u64 v[14:15], s[6:7], 0, v[14:15]
	v_lshl_add_u64 v[14:15], v[14:15], 0, v[18:19]
	v_pk_mul_f32 v[130:131], v[130:131], v[22:23]
	v_pk_mul_f32 v[132:133], v[132:133], v[24:25]
	v_pk_mul_f32 v[122:123], v[122:123], v[26:27]
	v_pk_mul_f32 v[124:125], v[124:125], v[28:29]
	v_pk_mul_f32 v[114:115], v[114:115], v[30:31]
	v_pk_mul_f32 v[116:117], v[116:117], v[32:33]
	v_pk_mul_f32 v[106:107], v[106:107], v[34:35]
	v_pk_mul_f32 v[108:109], v[108:109], v[36:37]
	v_cvt_pk_fp8_f32 v8, v130, v131
	v_cvt_pk_fp8_f32 v9, v122, v123
	v_cvt_pk_fp8_f32 v8, v132, v133 op_sel:[0,0,1]
	v_cvt_pk_fp8_f32 v9, v124, v125 op_sel:[0,0,1]
	v_cvt_pk_fp8_f32 v10, v114, v115
	v_cvt_pk_fp8_f32 v11, v106, v107
	v_cvt_pk_fp8_f32 v10, v116, v117 op_sel:[0,0,1]
	v_cvt_pk_fp8_f32 v11, v108, v109 op_sel:[0,0,1]
	s_nop 0
	global_store_dwordx2 v[12:13], v[8:9], off
	global_store_dwordx2 v[14:15], v[10:11], off
	v_pk_fma_f32 v[98:99], v[98:99], v[2:3], v[226:227] op_sel_hi:[1,0,1]
	v_pk_fma_f32 v[100:101], v[100:101], v[2:3], v[228:229] op_sel_hi:[1,0,1]
	v_pk_fma_f32 v[90:91], v[90:91], v[2:3], v[230:231] op_sel_hi:[1,0,1]
	v_pk_fma_f32 v[92:93], v[92:93], v[2:3], v[232:233] op_sel_hi:[1,0,1]
	v_pk_fma_f32 v[94:95], v[94:95], v[2:3], v[234:235] op_sel_hi:[1,0,1]
	v_pk_fma_f32 v[96:97], v[96:97], v[2:3], v[236:237] op_sel_hi:[1,0,1]
	v_pk_fma_f32 v[86:87], v[86:87], v[2:3], v[238:239] op_sel_hi:[1,0,1]
	v_pk_fma_f32 v[88:89], v[88:89], v[2:3], v[240:241] op_sel_hi:[1,0,1]
	v_pk_fma_f32 v[82:83], v[82:83], v[2:3], v[226:227] op_sel_hi:[1,0,1]
	v_pk_fma_f32 v[84:85], v[84:85], v[2:3], v[228:229] op_sel_hi:[1,0,1]
	v_pk_fma_f32 v[74:75], v[74:75], v[2:3], v[230:231] op_sel_hi:[1,0,1]
	v_pk_fma_f32 v[76:77], v[76:77], v[2:3], v[232:233] op_sel_hi:[1,0,1]
	v_pk_fma_f32 v[78:79], v[78:79], v[2:3], v[234:235] op_sel_hi:[1,0,1]
	v_pk_fma_f32 v[80:81], v[80:81], v[2:3], v[236:237] op_sel_hi:[1,0,1]
	v_pk_fma_f32 v[70:71], v[70:71], v[2:3], v[238:239] op_sel_hi:[1,0,1]
	v_pk_fma_f32 v[72:73], v[72:73], v[2:3], v[240:241] op_sel_hi:[1,0,1]
	v_min_f32_e32 v98, 0x40e00000, v98
	v_min_f32_e32 v99, 0x40e00000, v99
	v_min_f32_e32 v100, 0x40e00000, v100
	v_min_f32_e32 v101, 0x40e00000, v101
	v_min_f32_e32 v90, 0x40e00000, v90
	v_min_f32_e32 v91, 0x40e00000, v91
	v_min_f32_e32 v92, 0x40e00000, v92
	v_min_f32_e32 v93, 0x40e00000, v93
	v_med3_f32 v94, v94, s68, v221
	v_med3_f32 v95, v95, s68, v221
	v_med3_f32 v96, v96, s68, v221
	v_med3_f32 v97, v97, s68, v221
	v_med3_f32 v86, v86, s68, v221
	v_med3_f32 v87, v87, s68, v221
	v_med3_f32 v88, v88, s68, v221
	v_med3_f32 v89, v89, s68, v221
	v_min_f32_e32 v82, 0x40e00000, v82
	v_min_f32_e32 v83, 0x40e00000, v83
	v_min_f32_e32 v84, 0x40e00000, v84
	v_min_f32_e32 v85, 0x40e00000, v85
	v_min_f32_e32 v74, 0x40e00000, v74
	v_min_f32_e32 v75, 0x40e00000, v75
	v_min_f32_e32 v76, 0x40e00000, v76
	v_min_f32_e32 v77, 0x40e00000, v77
	v_med3_f32 v78, v78, s68, v221
	v_med3_f32 v79, v79, s68, v221
	v_med3_f32 v80, v80, s68, v221
	v_med3_f32 v81, v81, s68, v221
	v_med3_f32 v70, v70, s68, v221
	v_med3_f32 v71, v71, s68, v221
	v_med3_f32 v72, v72, s68, v221
	v_med3_f32 v73, v73, s68, v221
	v_pk_add_f32 v[94:95], v[94:95], 1.0 op_sel_hi:[1,0]
	v_pk_add_f32 v[96:97], v[96:97], 1.0 op_sel_hi:[1,0]
	v_pk_add_f32 v[86:87], v[86:87], 1.0 op_sel_hi:[1,0]
	v_pk_add_f32 v[88:89], v[88:89], 1.0 op_sel_hi:[1,0]
	v_pk_mul_f32 v[22:23], v[98:99], v[4:5] op_sel_hi:[1,0]
	v_pk_mul_f32 v[24:25], v[100:101], v[4:5] op_sel_hi:[1,0]
	v_pk_mul_f32 v[26:27], v[90:91], v[4:5] op_sel_hi:[1,0]
	v_pk_mul_f32 v[28:29], v[92:93], v[4:5] op_sel_hi:[1,0]
; __device__ __forceinline__ float sigmoidf_(float x) { return __builtin_amdgcn_rcpf(1.f + __builtin_amdgcn_exp2f(-1.4426950408889634f * x)); }
; __device__ __forceinline__ unsigned pack_fp8x4(float a, float b, float c, float d) { int w = __builtin_amdgcn_cvt_pk_fp8_f32(a, b, 0, false); w = __builtin_amdgcn_cvt_pk_fp8_f32(c, d, w, true); return (unsigned)w; }
; #define ACT(t) (KBASE(t) <= qlo + QBLK - 1 && KBASE(t) + KVBLK - 1 >= qlo - W + 1)
;     __device__ __forceinline__ void operator()(const f32x4 (&acc)[2][2][4][2], const Unit& u, int wr, int wc, int fr, int fq) const {
;     ...
; #pragma unroll
;                 for (int n = 0; n < 2; ++n)
; #pragma unroll
;                     for (int i = 0; i < 4; ++i) { float g = acc[ai][0][m][n][i] * 0.015625f + bg[n][i], up = acc[ai][1][m][n][i] * 0.015625f + bu[n][i];
;                         g = fminf(g, 7.0f); up = fminf(fmaxf(up, -7.0f), 7.0f);
;                         a[4 * n + i] = (up + 1.0f) * g * sigmoidf_(1.702f * g); }
;                 uint2 w; w.x = pack_fp8x4(a[0], a[1], a[2], a[3]); w.y = pack_fp8x4(a[4], a[5], a[6], a[7]);
;                 *(uint2*)(ACT + row * 2048 + colL) = w; }
	v_pk_add_f32 v[78:79], v[78:79], 1.0 op_sel_hi:[1,0]
	v_pk_add_f32 v[80:81], v[80:81], 1.0 op_sel_hi:[1,0]
	v_pk_add_f32 v[70:71], v[70:71], 1.0 op_sel_hi:[1,0]
	v_pk_add_f32 v[72:73], v[72:73], 1.0 op_sel_hi:[1,0]
	v_pk_mul_f32 v[30:31], v[82:83], v[4:5] op_sel_hi:[1,0]
	v_pk_mul_f32 v[32:33], v[84:85], v[4:5] op_sel_hi:[1,0]
	v_pk_mul_f32 v[34:35], v[74:75], v[4:5] op_sel_hi:[1,0]
	v_pk_mul_f32 v[36:37], v[76:77], v[4:5] op_sel_hi:[1,0]
	v_pk_mul_f32 v[22:23], v[22:23], v[6:7] op_sel_hi:[1,0]
	v_pk_mul_f32 v[24:25], v[24:25], v[6:7] op_sel_hi:[1,0]
	v_pk_mul_f32 v[26:27], v[26:27], v[6:7] op_sel_hi:[1,0]
	v_pk_mul_f32 v[28:29], v[28:29], v[6:7] op_sel_hi:[1,0]
	v_pk_mul_f32 v[30:31], v[30:31], v[6:7] op_sel_hi:[1,0]
	v_pk_mul_f32 v[32:33], v[32:33], v[6:7] op_sel_hi:[1,0]
	v_pk_mul_f32 v[34:35], v[34:35], v[6:7] op_sel_hi:[1,0]
	v_pk_mul_f32 v[36:37], v[36:37], v[6:7] op_sel_hi:[1,0]
	v_exp_f32_e32 v22, v22
	v_exp_f32_e32 v23, v23
	v_exp_f32_e32 v24, v24
	v_exp_f32_e32 v25, v25
	v_exp_f32_e32 v26, v26
	v_exp_f32_e32 v27, v27
	v_exp_f32_e32 v28, v28
	v_exp_f32_e32 v29, v29
	v_exp_f32_e32 v30, v30
	v_exp_f32_e32 v31, v31
	v_exp_f32_e32 v32, v32
	v_exp_f32_e32 v33, v33
	v_exp_f32_e32 v34, v34
	v_exp_f32_e32 v35, v35
	v_exp_f32_e32 v36, v36
	v_exp_f32_e32 v37, v37
	v_pk_mul_f32 v[98:99], v[98:99], v[94:95]
	v_pk_mul_f32 v[100:101], v[100:101], v[96:97]
	v_pk_mul_f32 v[90:91], v[90:91], v[86:87]
	v_pk_mul_f32 v[92:93], v[92:93], v[88:89]
	v_pk_mul_f32 v[82:83], v[82:83], v[78:79]
	v_pk_mul_f32 v[84:85], v[84:85], v[80:81]
	v_pk_mul_f32 v[74:75], v[74:75], v[70:71]
	v_pk_mul_f32 v[76:77], v[76:77], v[72:73]
	v_pk_add_f32 v[22:23], v[22:23], 1.0 op_sel_hi:[1,0]
	v_pk_add_f32 v[24:25], v[24:25], 1.0 op_sel_hi:[1,0]
	v_pk_add_f32 v[26:27], v[26:27], 1.0 op_sel_hi:[1,0]
	v_pk_add_f32 v[28:29], v[28:29], 1.0 op_sel_hi:[1,0]
	v_pk_add_f32 v[30:31], v[30:31], 1.0 op_sel_hi:[1,0]
	v_pk_add_f32 v[32:33], v[32:33], 1.0 op_sel_hi:[1,0]
	v_pk_add_f32 v[34:35], v[34:35], 1.0 op_sel_hi:[1,0]
	v_pk_add_f32 v[36:37], v[36:37], 1.0 op_sel_hi:[1,0]
	v_rcp_f32_e32 v22, v22
	v_rcp_f32_e32 v23, v23
	v_rcp_f32_e32 v24, v24
	v_rcp_f32_e32 v25, v25
	v_rcp_f32_e32 v26, v26
	v_rcp_f32_e32 v27, v27
	v_rcp_f32_e32 v28, v28
	v_rcp_f32_e32 v29, v29
	v_rcp_f32_e32 v30, v30
	v_rcp_f32_e32 v31, v31
	v_rcp_f32_e32 v32, v32
	v_rcp_f32_e32 v33, v33
	v_rcp_f32_e32 v34, v34
	v_rcp_f32_e32 v35, v35
	v_rcp_f32_e32 v36, v36
	v_rcp_f32_e32 v37, v37
	v_add_u32_e32 v12, 0xa0, v20
	v_ashrrev_i32_e32 v13, 31, v12
	v_lshlrev_b64 v[12:13], 11, v[12:13]
	v_lshl_add_u64 v[12:13], s[6:7], 0, v[12:13]
	v_lshl_add_u64 v[12:13], v[12:13], 0, v[18:19]
	v_add_u32_e32 v14, 0xb0, v20
	v_ashrrev_i32_e32 v15, 31, v14
	v_lshlrev_b64 v[14:15], 11, v[14:15]
	v_lshl_add_u64 v[14:15], s[6:7], 0, v[14:15]
	v_lshl_add_u64 v[14:15], v[14:15], 0, v[18:19]
	v_pk_mul_f32 v[98:99], v[98:99], v[22:23]
	v_pk_mul_f32 v[100:101], v[100:101], v[24:25]
	v_pk_mul_f32 v[90:91], v[90:91], v[26:27]
	v_pk_mul_f32 v[92:93], v[92:93], v[28:29]
	v_pk_mul_f32 v[82:83], v[82:83], v[30:31]
	v_pk_mul_f32 v[84:85], v[84:85], v[32:33]
	v_pk_mul_f32 v[74:75], v[74:75], v[34:35]
	v_pk_mul_f32 v[76:77], v[76:77], v[36:37]
	v_cvt_pk_fp8_f32 v8, v98, v99
	v_cvt_pk_fp8_f32 v9, v90, v91
	v_cvt_pk_fp8_f32 v8, v100, v101 op_sel:[0,0,1]
	v_cvt_pk_fp8_f32 v9, v92, v93 op_sel:[0,0,1]
	v_cvt_pk_fp8_f32 v10, v82, v83
	v_cvt_pk_fp8_f32 v11, v74, v75
	v_cvt_pk_fp8_f32 v10, v84, v85 op_sel:[0,0,1]
	v_cvt_pk_fp8_f32 v11, v76, v77 op_sel:[0,0,1]
	s_nop 0
	global_store_dwordx2 v[12:13], v[8:9], off
	global_store_dwordx2 v[14:15], v[10:11], off
	s_andn2_b64 vcc, exec, s[26:27]
	s_mov_b64 s[2:3], -1
	s_cbranch_vccnz .LBB0_1334
